# v8 + cross-barrier prefetch: P9 build H2Q row loads and P7 key-table loads issued before their grid barrier (entry wait keeps the 16 newest ops in flight)
# speedup vs baseline: 1.0001x; 1.0001x over previous
; #define GAS __attribute__((address_space(1)))
; #define LAS __attribute__((address_space(3)))
; DI unsigned pk2(float lo, float hi) { return f2bf(lo) | (f2bf(hi) << 16); }
; __device__ __forceinline__ unsigned xb_add(unsigned* p, unsigned v) { return __hip_atomic_fetch_add(p, v, __ATOMIC_RELAXED, __HIP_MEMORY_SCOPE_AGENT); }
; __device__ __forceinline__ void xcd_barrier(const XcdBarrier& b) {
;     asm volatile("s_waitcnt vmcnt(0)" ::: "memory");
;     __syncthreads();
;     if (threadIdx.x == 0) {
;         unsigned* bar = b.bar;
;         __builtin_amdgcn_s_waitcnt(0);
;         unsigned nloc = b.st[0], nx = b.st[1];
;         if (nloc == 0u) { xcd_barrier_complete(bar, b.x, nloc, nx); b.st[0] = nloc; b.st[1] = nx; }
;         const unsigned old = xb_add(&bar[XB_XSUB(b.x)], 1u);
;         const unsigned gen = old / nloc;
;         if (old + 1u == (gen + 1u) * nloc) {
; DI void p8_phase(Frame& F) {
;     ...
; #pragma unroll 4
;     for (int i = 0; i < 16; ++i) { const int idx = tid * 4 + 2048 * i, side = idx >> 14, rem = idx & 16383, row = rem >> 7, col = rem & 127;
;         const f32x4 a = *(const GAS f32x4*)((side ? F.keys2 : F.keys1) + rem);
;         v2u o; o.x = pk2(a.x, a.y); o.y = pk2(a.z, a.w); *(LAS v2u*)(KIMG + (side * 128 + row) * KPITCH + col * 2) = o; }
.LBB0_1151:
	s_mov_b32 s85, 0
	s_movk_i32 s86, 0x4000
	s_mov_b32 s84, 0
	v_mov_b32_e32 v3, 0
	v_mov_b32_e32 v7, s79
	v_mov_b32_e32 v8, s77
	v_mov_b32_e32 v9, s78
	v_mov_b32_e32 v10, s76
	v_add_u32_e32 v2, s85, v150
	s_cmp_lt_u32 s84, 8
	v_and_b32_e32 v11, 0x2ffc, v2
	v_add_u32_e32 v40, 0x800, v2
	v_add_u32_e32 v41, 0x1000, v2
	s_cselect_b32 s91, s77, s79
	s_cselect_b32 s90, s76, s78
	s_cmpk_lt_u32 s85, 0x4000
	v_add_u32_e32 v2, 0x1800, v2
	v_lshlrev_b32_e32 v11, 2, v11
	v_and_b32_e32 v44, 0x3ffc, v40
	v_cmp_gt_u32_e32 vcc, s86, v40
	v_and_b32_e32 v45, 0x3ffc, v41
	s_cselect_b32 s93, s77, s79
	v_cndmask_b32_e32 v49, v7, v8, vcc
	s_cselect_b32 s92, s76, s78
	v_and_b32_e32 v50, 0x3ffc, v2
	v_cmp_gt_u32_e64 s[94:95], s86, v2
	global_load_dwordx4 v[40:43], v11, s[90:91]
	v_cndmask_b32_e32 v48, v9, v10, vcc
	v_lshlrev_b32_e32 v2, 2, v44
	v_lshlrev_b32_e32 v11, 2, v45
	v_cndmask_b32_e64 v53, v7, v8, s[94:95]
	v_cndmask_b32_e64 v52, v9, v10, s[94:95]
	global_load_dwordx4 v[44:47], v11, s[92:93]
	v_lshl_add_u64 v[48:49], v[48:49], 0, v[2:3]
	v_lshlrev_b32_e32 v2, 2, v50
	global_load_dwordx4 v[48:51], v[48:49], off
	v_lshl_add_u64 v[52:53], v[52:53], 0, v[2:3]
	global_load_dwordx4 v[52:55], v[52:53], off
	s_add_i32 s84, s84, 4
	s_addk_i32 s85, 0x2000
	s_cmpk_eq_u32 s85, 0x8000
	v_add_u32_e32 v2, s85, v150
	s_cmp_lt_u32 s84, 8
	v_and_b32_e32 v11, 0x2ffc, v2
	v_add_u32_e32 v56, 0x800, v2
	v_add_u32_e32 v57, 0x1000, v2
	s_cselect_b32 s91, s77, s79
	s_cselect_b32 s90, s76, s78
	s_cmpk_lt_u32 s85, 0x4000
	v_add_u32_e32 v2, 0x1800, v2
	v_lshlrev_b32_e32 v11, 2, v11
	v_and_b32_e32 v60, 0x3ffc, v56
	v_cmp_gt_u32_e32 vcc, s86, v56
	v_and_b32_e32 v61, 0x3ffc, v57
	s_cselect_b32 s93, s77, s79
	v_cndmask_b32_e32 v65, v7, v8, vcc
	s_cselect_b32 s92, s76, s78
	v_and_b32_e32 v66, 0x3ffc, v2
	v_cmp_gt_u32_e64 s[94:95], s86, v2
	global_load_dwordx4 v[56:59], v11, s[90:91]
	v_cndmask_b32_e32 v64, v9, v10, vcc
	v_lshlrev_b32_e32 v2, 2, v60
	v_lshlrev_b32_e32 v11, 2, v61
	v_cndmask_b32_e64 v69, v7, v8, s[94:95]
	v_cndmask_b32_e64 v68, v9, v10, s[94:95]
	global_load_dwordx4 v[60:63], v11, s[92:93]
	v_lshl_add_u64 v[64:65], v[64:65], 0, v[2:3]
	v_lshlrev_b32_e32 v2, 2, v66
	global_load_dwordx4 v[64:67], v[64:65], off
	v_lshl_add_u64 v[68:69], v[68:69], 0, v[2:3]
	global_load_dwordx4 v[68:71], v[68:69], off
	s_add_i32 s84, s84, 4
	s_addk_i32 s85, 0x2000
	s_cmpk_eq_u32 s85, 0x8000
	v_add_u32_e32 v2, s85, v150
	s_cmp_lt_u32 s84, 8
	v_and_b32_e32 v11, 0x2ffc, v2
	v_add_u32_e32 v72, 0x800, v2
	v_add_u32_e32 v73, 0x1000, v2
	s_cselect_b32 s91, s77, s79
	s_cselect_b32 s90, s76, s78
	s_cmpk_lt_u32 s85, 0x4000
	v_add_u32_e32 v2, 0x1800, v2
	v_lshlrev_b32_e32 v11, 2, v11
	v_and_b32_e32 v76, 0x3ffc, v72
	v_cmp_gt_u32_e32 vcc, s86, v72
	v_and_b32_e32 v77, 0x3ffc, v73
	s_cselect_b32 s93, s77, s79
	v_cndmask_b32_e32 v81, v7, v8, vcc
	s_cselect_b32 s92, s76, s78
	v_and_b32_e32 v82, 0x3ffc, v2
	v_cmp_gt_u32_e64 s[94:95], s86, v2
	global_load_dwordx4 v[72:75], v11, s[90:91]
	v_cndmask_b32_e32 v80, v9, v10, vcc
	v_lshlrev_b32_e32 v2, 2, v76
	v_lshlrev_b32_e32 v11, 2, v77
	v_cndmask_b32_e64 v85, v7, v8, s[94:95]
	v_cndmask_b32_e64 v84, v9, v10, s[94:95]
	global_load_dwordx4 v[76:79], v11, s[92:93]
	v_lshl_add_u64 v[80:81], v[80:81], 0, v[2:3]
	v_lshlrev_b32_e32 v2, 2, v82
	global_load_dwordx4 v[80:83], v[80:81], off
	v_lshl_add_u64 v[84:85], v[84:85], 0, v[2:3]
	global_load_dwordx4 v[84:87], v[84:85], off
	s_add_i32 s84, s84, 4
	s_addk_i32 s85, 0x2000
	s_cmpk_eq_u32 s85, 0x8000
	v_add_u32_e32 v2, s85, v150
	s_cmp_lt_u32 s84, 8
	v_and_b32_e32 v11, 0x2ffc, v2
	v_add_u32_e32 v88, 0x800, v2
	v_add_u32_e32 v89, 0x1000, v2
	s_cselect_b32 s91, s77, s79
	s_cselect_b32 s90, s76, s78
	s_cmpk_lt_u32 s85, 0x4000
	v_add_u32_e32 v2, 0x1800, v2
	v_lshlrev_b32_e32 v11, 2, v11
	v_and_b32_e32 v92, 0x3ffc, v88
	v_cmp_gt_u32_e32 vcc, s86, v88
	v_and_b32_e32 v93, 0x3ffc, v89
	s_cselect_b32 s93, s77, s79
	v_cndmask_b32_e32 v97, v7, v8, vcc
	s_cselect_b32 s92, s76, s78
	v_and_b32_e32 v98, 0x3ffc, v2
	v_cmp_gt_u32_e64 s[94:95], s86, v2
	global_load_dwordx4 v[88:91], v11, s[90:91]
	v_cndmask_b32_e32 v96, v9, v10, vcc
	v_lshlrev_b32_e32 v2, 2, v92
	v_lshlrev_b32_e32 v11, 2, v93
	v_cndmask_b32_e64 v101, v7, v8, s[94:95]
	v_cndmask_b32_e64 v100, v9, v10, s[94:95]
	global_load_dwordx4 v[92:95], v11, s[92:93]
	v_lshl_add_u64 v[96:97], v[96:97], 0, v[2:3]
	v_lshlrev_b32_e32 v2, 2, v98
	global_load_dwordx4 v[96:99], v[96:97], off
	v_lshl_add_u64 v[100:101], v[100:101], 0, v[2:3]
	global_load_dwordx4 v[100:103], v[100:101], off
	s_add_i32 s84, s84, 4
	s_addk_i32 s85, 0x2000
	s_cmpk_eq_u32 s85, 0x8000
	v_readlane_b32 s0, v252, 4
	v_readlane_b32 s1, v252, 5
	s_cmp_gt_i32 s1, 8
	v_readlane_b32 s2, v252, 6
	v_readlane_b32 s3, v252, 7
	s_cselect_b64 s[0:1], -1, 0
	s_and_b64 s[2:3], s[6:7], s[0:1]
	s_andn2_b64 vcc, exec, s[2:3]
	s_cbranch_vccnz .LBB0_1201
	s_waitcnt vmcnt(16)
	v_cmp_eq_u32_e32 vcc, 0, v0
	s_waitcnt lgkmcnt(0)
	s_barrier
	s_and_saveexec_b64 s[2:3], vcc
	s_cbranch_execz .LBB0_1200
	v_readlane_b32 s4, v252, 38
	s_waitcnt vmcnt(0) expcnt(0) lgkmcnt(0)
	s_nop 0
	v_mov_b32_e32 v1, s4
	ds_read_b32 v3, v1
	ds_read_b32 v1, v1 offset:4
	s_waitcnt lgkmcnt(1)
	v_cmp_ne_u32_e32 vcc, 0, v3
	s_cbranch_vccnz .LBB0_1168
	v_readlane_b32 s4, v252, 9
	v_readlane_b32 s5, v252, 10
	s_load_dwordx2 s[8:9], s[4:5], 0x4
	v_readlane_b32 s4, v252, 35
	v_readlane_b32 s5, v252, 36
	s_lshl_b64 s[4:5], s[4:5], 2
	v_readlane_b32 s6, v252, 33
	s_add_u32 s4, s6, s4
	v_readlane_b32 s6, v252, 34
	s_addc_u32 s5, s6, s5
	s_add_u32 s6, s4, 0x1000
	v_readlane_b32 s7, v252, 11
	s_waitcnt lgkmcnt(0)
	s_mul_i32 s20, s8, s7
	s_addc_u32 s7, s5, 0
	s_add_u32 s8, s4, 0x1100
	s_mul_i32 s20, s20, s9
	s_addc_u32 s9, s5, 0
	s_add_u32 s10, s4, 0x1200
	s_addc_u32 s11, s5, 0
	s_add_u32 s12, s4, 0x1300
	s_addc_u32 s13, s5, 0
	s_mov_b32 s21, 1
	v_mov_b32_e32 v17, 0
	s_branch .LBB0_1156

; #define GAS __attribute__((address_space(1)))
; #define LAS __attribute__((address_space(3)))
; DI unsigned pk2(float lo, float hi) { return f2bf(lo) | (f2bf(hi) << 16); }
; DI void p8_phase(Frame& F) {
;     LAS unsigned char* KIMG = F.lds; LAS unsigned char* TBL = F.lds + P8_TBL + F.wave * 1024;
;     const int lane = F.lane, tid = F.tid, r = lane & 31, h = lane >> 5;
; #pragma unroll 4
;     for (int i = 0; i < 16; ++i) { const int idx = tid * 4 + 2048 * i, side = idx >> 14, rem = idx & 16383, row = rem >> 7, col = rem & 127;
;         const f32x4 a = *(const GAS f32x4*)((side ? F.keys2 : F.keys1) + rem);
;         v2u o; o.x = pk2(a.x, a.y); o.y = pk2(a.z, a.w); *(LAS v2u*)(KIMG + (side * 128 + row) * KPITCH + col * 2) = o; }
;     __syncthreads();
.LBB0_1201:
	v_readlane_b32 s4, v252, 4
	v_readlane_b32 s5, v252, 5
	s_cmp_lt_i32 s4, 9
	v_readlane_b32 s4, v252, 13
	s_cselect_b64 s[2:3], -1, 0
	v_readlane_b32 s5, v252, 14
	s_add_u32 s14, s4, 0x3400000
	s_addc_u32 s15, s5, 0
	s_add_u32 s16, s4, 0x2c00000
	s_addc_u32 s17, s5, 0
	s_add_u32 s37, s4, 0x18000000
	s_addc_u32 s39, s5, 0
	s_add_u32 s18, s4, 0x1a000000
	s_addc_u32 s19, s5, 0
	s_add_u32 s20, s4, 0x380000
	s_addc_u32 s21, s5, 0
	s_add_u32 s24, s4, 0x390000
	s_addc_u32 s25, s5, 0
	s_and_b64 s[8:9], s[2:3], s[0:1]
	s_andn2_b64 vcc, exec, s[8:9]
	v_readlane_b32 s6, v252, 6
	v_readlane_b32 s7, v252, 7
	s_cbranch_vccnz .LBB0_1246
	v_lshlrev_b32_e32 v1, 3, v0
	v_lshrrev_b32_e32 v3, 5, v0
	s_waitcnt lgkmcnt(0)
	v_and_b32_e32 v2, 0xf8, v1
	v_or_b32_e32 v1, 48, v3
	v_or_b32_e32 v4, 32, v3
	v_or_b32_e32 v5, 16, v3
	v_mul_u32_u24_e32 v1, 0x110, v1
	v_mul_u32_u24_e32 v4, 0x110, v4
	v_mul_u32_u24_e32 v5, 0x110, v5
	v_mul_u32_u24_e32 v3, 0x110, v3
	s_mov_b32 s2, 0
	v_add3_u32 v1, v1, v2, 0
	v_add3_u32 v4, v4, v2, 0
	v_add3_u32 v5, v5, v2, 0
	v_add3_u32 v6, v3, v2, 0
	s_movk_i32 s3, 0x7fff
	s_mov_b32 s4, 0xffff0000
	s_movk_i32 s5, 0x4000
	v_mov_b32_e32 v7, s79
	s_waitcnt vmcnt(31)
	v_mov_b32_e32 v8, s77
	s_waitcnt vmcnt(30)
	v_mov_b32_e32 v9, s78
	v_mov_b32_e32 v10, s76
	v_mov_b32_e32 v3, 0
	s_mov_b32 s6, 0
	s_waitcnt vmcnt(15)
	v_bfe_u32 v2, v40, 16, 1
	v_bfe_u32 v28, v42, 16, 1
	v_bfe_u32 v11, v41, 16, 1
	v_bfe_u32 v29, v43, 16, 1
	v_add3_u32 v2, v40, v2, s3
	v_add3_u32 v40, v42, v28, s3
	s_waitcnt vmcnt(14)
	v_bfe_u32 v42, v44, 16, 1
	v_bfe_u32 v28, v46, 16, 1
	v_add3_u32 v11, v41, v11, s3
	v_add3_u32 v41, v43, v29, s3
	v_bfe_u32 v43, v45, 16, 1
	v_bfe_u32 v29, v47, 16, 1
	v_lshrrev_b32_e32 v2, 16, v2
	v_lshrrev_b32_e32 v30, 16, v40
	s_waitcnt vmcnt(13)
	v_bfe_u32 v31, v48, 16, 1
	v_bfe_u32 v33, v50, 16, 1
	v_add3_u32 v42, v44, v42, s3
	v_add3_u32 v44, v46, v28, s3
	v_bfe_u32 v32, v49, 16, 1
	v_bfe_u32 v34, v51, 16, 1
	v_add3_u32 v43, v45, v43, s3
	v_add3_u32 v45, v47, v29, s3
	v_and_or_b32 v40, v11, s4, v2
	v_and_or_b32 v41, v41, s4, v30
	v_add3_u32 v2, v48, v31, s3
	v_add3_u32 v46, v50, v33, s3
	v_lshrrev_b32_e32 v44, 16, v44
	s_waitcnt vmcnt(12)
	v_bfe_u32 v48, v52, 16, 1
	v_bfe_u32 v50, v54, 16, 1
	v_add3_u32 v11, v49, v32, s3
	v_add3_u32 v47, v51, v34, s3
	v_lshrrev_b32_e32 v42, 16, v42
	v_bfe_u32 v49, v53, 16, 1
	v_bfe_u32 v51, v55, 16, 1
	ds_write_b64 v6, v[40:41]
	v_lshrrev_b32_e32 v2, 16, v2
	v_lshrrev_b32_e32 v46, 16, v46
	v_and_or_b32 v41, v45, s4, v44
	v_add3_u32 v44, v52, v48, s3
	v_add3_u32 v48, v54, v50, s3
	v_and_or_b32 v40, v43, s4, v42
	v_add3_u32 v45, v53, v49, s3
	v_add3_u32 v49, v55, v51, s3
	v_and_or_b32 v42, v11, s4, v2
	v_and_or_b32 v43, v47, s4, v46
	v_lshrrev_b32_e32 v2, 16, v44
	v_lshrrev_b32_e32 v11, 16, v48
	ds_write_b64 v5, v[42:43]
	ds_write_b64 v4, v[40:41]
	v_and_or_b32 v40, v45, s4, v2
	v_and_or_b32 v41, v49, s4, v11
	ds_write_b64 v1, v[40:41]
	s_waitcnt vmcnt(11)
	v_bfe_u32 v2, v56, 16, 1
	v_bfe_u32 v28, v58, 16, 1
	v_bfe_u32 v11, v57, 16, 1
	v_bfe_u32 v29, v59, 16, 1
	v_add3_u32 v2, v56, v2, s3
	v_add3_u32 v56, v58, v28, s3
	s_waitcnt vmcnt(10)
	v_bfe_u32 v58, v60, 16, 1
	v_bfe_u32 v28, v62, 16, 1
	v_add3_u32 v11, v57, v11, s3
	v_add3_u32 v57, v59, v29, s3
	v_bfe_u32 v59, v61, 16, 1
	v_bfe_u32 v29, v63, 16, 1
	v_lshrrev_b32_e32 v2, 16, v2
	v_lshrrev_b32_e32 v30, 16, v56
	s_waitcnt vmcnt(9)
	v_bfe_u32 v31, v64, 16, 1
	v_bfe_u32 v33, v66, 16, 1
	v_add3_u32 v58, v60, v58, s3
	v_add3_u32 v60, v62, v28, s3
	v_bfe_u32 v32, v65, 16, 1
	v_bfe_u32 v34, v67, 16, 1
	v_add3_u32 v59, v61, v59, s3
	v_add3_u32 v61, v63, v29, s3
	v_and_or_b32 v56, v11, s4, v2
	v_and_or_b32 v57, v57, s4, v30
	v_add3_u32 v2, v64, v31, s3
	v_add3_u32 v62, v66, v33, s3
	v_lshrrev_b32_e32 v60, 16, v60
	s_waitcnt vmcnt(8)
	v_bfe_u32 v64, v68, 16, 1
	v_bfe_u32 v66, v70, 16, 1
	v_add3_u32 v11, v65, v32, s3
	v_add3_u32 v63, v67, v34, s3
	v_lshrrev_b32_e32 v58, 16, v58
	v_bfe_u32 v65, v69, 16, 1
	v_bfe_u32 v67, v71, 16, 1
	ds_write_b64 v6, v[56:57] offset:17408
	v_lshrrev_b32_e32 v2, 16, v2
	v_lshrrev_b32_e32 v62, 16, v62
	v_and_or_b32 v57, v61, s4, v60
	v_add3_u32 v60, v68, v64, s3
	v_add3_u32 v64, v70, v66, s3
	v_and_or_b32 v56, v59, s4, v58
	v_add3_u32 v61, v69, v65, s3
	v_add3_u32 v65, v71, v67, s3
	v_and_or_b32 v58, v11, s4, v2
	v_and_or_b32 v59, v63, s4, v62
	v_lshrrev_b32_e32 v2, 16, v60
	v_lshrrev_b32_e32 v11, 16, v64
	ds_write_b64 v5, v[58:59] offset:17408
	ds_write_b64 v4, v[56:57] offset:17408
	v_and_or_b32 v56, v61, s4, v2
	v_and_or_b32 v57, v65, s4, v11
	ds_write_b64 v1, v[56:57] offset:17408
	s_waitcnt vmcnt(7)
	v_bfe_u32 v2, v72, 16, 1
	v_bfe_u32 v28, v74, 16, 1
	v_bfe_u32 v11, v73, 16, 1
	v_bfe_u32 v29, v75, 16, 1
	v_add3_u32 v2, v72, v2, s3
	v_add3_u32 v72, v74, v28, s3
	s_waitcnt vmcnt(6)
	v_bfe_u32 v74, v76, 16, 1
	v_bfe_u32 v28, v78, 16, 1
	v_add3_u32 v11, v73, v11, s3
	v_add3_u32 v73, v75, v29, s3
	v_bfe_u32 v75, v77, 16, 1
	v_bfe_u32 v29, v79, 16, 1
	v_lshrrev_b32_e32 v2, 16, v2
	v_lshrrev_b32_e32 v30, 16, v72
	s_waitcnt vmcnt(5)
	v_bfe_u32 v31, v80, 16, 1
	v_bfe_u32 v33, v82, 16, 1
	v_add3_u32 v74, v76, v74, s3
	v_add3_u32 v76, v78, v28, s3
	v_bfe_u32 v32, v81, 16, 1
	v_bfe_u32 v34, v83, 16, 1
	v_add3_u32 v75, v77, v75, s3
	v_add3_u32 v77, v79, v29, s3
	v_and_or_b32 v72, v11, s4, v2
	v_and_or_b32 v73, v73, s4, v30
	v_add3_u32 v2, v80, v31, s3
	v_add3_u32 v78, v82, v33, s3
	v_lshrrev_b32_e32 v76, 16, v76
	s_waitcnt vmcnt(4)
; #define GAS __attribute__((address_space(1)))
; #define LAS __attribute__((address_space(3)))
; DI unsigned pk2(float lo, float hi) { return f2bf(lo) | (f2bf(hi) << 16); }
; DI f32x16 zero16() { f32x16 z; for (int i = 0; i < 16; ++i) z[i] = 0.f; return z; }
; DI void p8_phase(Frame& F) {
;     ...
;     for (int i = 0; i < 16; ++i) { const int idx = tid * 4 + 2048 * i, side = idx >> 14, rem = idx & 16383, row = rem >> 7, col = rem & 127;
;         const f32x4 a = *(const GAS f32x4*)((side ? F.keys2 : F.keys1) + rem);
;         v2u o; o.x = pk2(a.x, a.y); o.y = pk2(a.z, a.w); *(LAS v2u*)(KIMG + (side * 128 + row) * KPITCH + col * 2) = o; }
;     __syncthreads();
;     const int gcT = F.vcu * NWAVES + F.wave, NGWT = F.G * NWAVES; int trow_it = 0;
;     for (int it = (int)blockIdx.x; it < (M / 256) * PH; it += F.G, ++trow_it) {
;         const int tile = it / PH, hd = it % PH;
;         const int t = tile * 256 + F.wave * 32 + r;
;         float L1[16], L2[16];
; #pragma unroll 1
;         for (int side = 0; side < 2; ++side) {
;             const int q0 = (trow_it * 2 + side) * 4; f32x4 ra[8], rb[8];
;             f32x16 acc[4];
; #pragma unroll
;             for (int kt = 0; kt < 4; ++kt) acc[kt] = zero16();
;             const bf16* qp = F.QB + (size_t)t * D + hd * 256 + side * 128 + 8 * h;
	v_bfe_u32 v80, v84, 16, 1
	v_bfe_u32 v82, v86, 16, 1
	v_add3_u32 v11, v81, v32, s3
	v_add3_u32 v79, v83, v34, s3
	v_lshrrev_b32_e32 v74, 16, v74
	v_bfe_u32 v81, v85, 16, 1
	v_bfe_u32 v83, v87, 16, 1
	ds_write_b64 v6, v[72:73] offset:34816
	v_lshrrev_b32_e32 v2, 16, v2
	v_lshrrev_b32_e32 v78, 16, v78
	v_and_or_b32 v73, v77, s4, v76
	v_add3_u32 v76, v84, v80, s3
	v_add3_u32 v80, v86, v82, s3
	v_and_or_b32 v72, v75, s4, v74
	v_add3_u32 v77, v85, v81, s3
	v_add3_u32 v81, v87, v83, s3
	v_and_or_b32 v74, v11, s4, v2
	v_and_or_b32 v75, v79, s4, v78
	v_lshrrev_b32_e32 v2, 16, v76
	v_lshrrev_b32_e32 v11, 16, v80
	ds_write_b64 v5, v[74:75] offset:34816
	ds_write_b64 v4, v[72:73] offset:34816
	v_and_or_b32 v72, v77, s4, v2
	v_and_or_b32 v73, v81, s4, v11
	ds_write_b64 v1, v[72:73] offset:34816
	s_waitcnt vmcnt(3)
	v_bfe_u32 v2, v88, 16, 1
	v_bfe_u32 v28, v90, 16, 1
	v_bfe_u32 v11, v89, 16, 1
	v_bfe_u32 v29, v91, 16, 1
	v_add3_u32 v2, v88, v2, s3
	v_add3_u32 v88, v90, v28, s3
	s_waitcnt vmcnt(2)
	v_bfe_u32 v90, v92, 16, 1
	v_bfe_u32 v28, v94, 16, 1
	v_add3_u32 v11, v89, v11, s3
	v_add3_u32 v89, v91, v29, s3
	v_bfe_u32 v91, v93, 16, 1
	v_bfe_u32 v29, v95, 16, 1
	v_lshrrev_b32_e32 v2, 16, v2
	v_lshrrev_b32_e32 v30, 16, v88
	s_waitcnt vmcnt(1)
	v_bfe_u32 v31, v96, 16, 1
	v_bfe_u32 v33, v98, 16, 1
	v_add3_u32 v90, v92, v90, s3
	v_add3_u32 v92, v94, v28, s3
	v_bfe_u32 v32, v97, 16, 1
	v_bfe_u32 v34, v99, 16, 1
	v_add3_u32 v91, v93, v91, s3
	v_add3_u32 v93, v95, v29, s3
	v_and_or_b32 v88, v11, s4, v2
	v_and_or_b32 v89, v89, s4, v30
	v_add3_u32 v2, v96, v31, s3
	v_add3_u32 v94, v98, v33, s3
	v_lshrrev_b32_e32 v92, 16, v92
	s_waitcnt vmcnt(0)
	v_bfe_u32 v96, v100, 16, 1
	v_bfe_u32 v98, v102, 16, 1
	v_add3_u32 v11, v97, v32, s3
	v_add3_u32 v95, v99, v34, s3
	v_lshrrev_b32_e32 v90, 16, v90
	v_bfe_u32 v97, v101, 16, 1
	v_bfe_u32 v99, v103, 16, 1
	ds_write_b64 v6, v[88:89] offset:52224
	v_lshrrev_b32_e32 v2, 16, v2
	v_lshrrev_b32_e32 v94, 16, v94
	v_and_or_b32 v89, v93, s4, v92
	v_add3_u32 v92, v100, v96, s3
	v_add3_u32 v96, v102, v98, s3
	v_and_or_b32 v88, v91, s4, v90
	v_add3_u32 v93, v101, v97, s3
	v_add3_u32 v97, v103, v99, s3
	v_and_or_b32 v90, v11, s4, v2
	v_and_or_b32 v91, v95, s4, v94
	v_lshrrev_b32_e32 v2, 16, v92
	v_lshrrev_b32_e32 v11, 16, v96
	ds_write_b64 v5, v[90:91] offset:52224
	ds_write_b64 v4, v[88:89] offset:52224
	v_and_or_b32 v88, v93, s4, v2
	v_and_or_b32 v89, v97, s4, v11
	ds_write_b64 v1, v[88:89] offset:52224
	v_add_u32_e32 v6, 0x11000, v6
	v_add_u32_e32 v4, 0x11000, v4
	v_add_u32_e32 v5, 0x11000, v5
	v_add_u32_e32 v1, 0x11000, v1
	v_readlane_b32 s0, v252, 12
	s_lshl_b32 s35, s0, 3
	v_readlane_b32 s0, v252, 11
	s_lshl_b32 s34, s0, 3
	s_andn2_b64 vcc, exec, s[22:23]
	s_mov_b32 s10, 0
	s_waitcnt lgkmcnt(0)
	s_barrier
	s_cbranch_vccnz .LBB0_1237
	v_mbcnt_hi_u32_b32 v1, -1, v200
	v_and_b32_e32 v3, 64, v1
	v_xor_b32_e32 v2, 32, v1
	v_add_u32_e32 v3, 64, v3
	s_lshl_b32 s0, s89, 10
	v_cmp_lt_i32_e32 vcc, v2, v3
	s_add_i32 s0, s0, 0
	s_add_i32 s2, s0, 0x11000
	v_cndmask_b32_e32 v1, v1, v2, vcc
	v_lshlrev_b32_e32 v130, 3, v197
	v_lshlrev_b32_e32 v131, 2, v197
	v_lshlrev_b32_e32 v137, 2, v1
	v_lshlrev_b32_e32 v1, 5, v148
	s_add_i32 s36, s35, s89
	s_mov_b32 s11, 0
	v_mov_b32_e32 v133, 0
	v_cmp_gt_u32_e64 s[0:1], 32, v148
	v_cmp_lt_u32_e64 s[6:7], 31, v148
	v_lshl_add_u32 v139, v149, 5, s2
	v_lshl_add_u32 v144, v197, 4, 0
	v_lshl_or_b32 v145, s89, 5, v149
	v_cmp_eq_u32_e64 s[4:5], 0, v148
	v_or_b32_e32 v147, 1, v131
	v_or_b32_e32 v151, 2, v131
	v_or_b32_e32 v152, 3, v131
	v_or_b32_e32 v153, 8, v131
	v_or_b32_e32 v154, 9, v131
	v_or_b32_e32 v155, 10, v131
	v_or_b32_e32 v156, 11, v131
	v_or_b32_e32 v157, 16, v131
	v_or_b32_e32 v158, 17, v131
	v_or_b32_e32 v159, 18, v131
	v_or_b32_e32 v160, 19, v131
	v_or_b32_e32 v161, 24, v131
	v_or_b32_e32 v162, 25, v131
	v_or_b32_e32 v163, 26, v131
	v_or_b32_e32 v164, 27, v131
	v_or_b32_e32 v165, 32, v131
	v_or_b32_e32 v166, 33, v131
	v_or_b32_e32 v167, 34, v131
	v_or_b32_e32 v168, 35, v131
	v_or_b32_e32 v169, 40, v131
	v_or_b32_e32 v170, 41, v131
	v_or_b32_e32 v171, 42, v131
	v_or_b32_e32 v172, 43, v131
	v_or_b32_e32 v173, 48, v131
	v_or_b32_e32 v174, 49, v131
	v_or_b32_e32 v175, 50, v131
	v_or_b32_e32 v176, 51, v131
	v_or_b32_e32 v177, 56, v131
	v_or_b32_e32 v178, 57, v131
	v_or_b32_e32 v179, 58, v131
	v_or_b32_e32 v180, 59, v131
	v_or_b32_e32 v181, 64, v131
	v_or_b32_e32 v182, 0x41, v131
	v_or_b32_e32 v183, 0x42, v131
	v_or_b32_e32 v184, 0x43, v131
	v_or_b32_e32 v185, 0x48, v131
	v_or_b32_e32 v186, 0x49, v131
	v_or_b32_e32 v187, 0x4a, v131
	v_or_b32_e32 v188, 0x4b, v131
	v_or_b32_e32 v189, 0x50, v131
	v_or_b32_e32 v190, 0x51, v131
	v_or_b32_e32 v191, 0x52, v131
	v_or_b32_e32 v192, 0x53, v131
	v_or_b32_e32 v193, 0x58, v131
	v_or_b32_e32 v194, 0x59, v131
	v_or_b32_e32 v195, 0x5a, v131
	v_or_b32_e32 v196, 0x5b, v131
	v_or_b32_e32 v198, 0x60, v131
	v_or_b32_e32 v199, 0x61, v131
	v_or_b32_e32 v201, 0x62, v131
	v_or_b32_e32 v202, 0x63, v131
	v_or_b32_e32 v203, 0x68, v131
	v_or_b32_e32 v204, 0x69, v131
	v_or_b32_e32 v205, 0x6a, v131
	v_or_b32_e32 v206, 0x6b, v131
	v_or_b32_e32 v207, 0x70, v131
	v_or_b32_e32 v208, 0x71, v131
	v_or_b32_e32 v209, 0x72, v131
	v_or_b32_e32 v210, 0x73, v131
	v_or_b32_e32 v211, 0x78, v131
	v_or_b32_e32 v212, 0x79, v131
	v_or_b32_e32 v213, 0x7a, v131
	v_or_b32_e32 v214, 0x7b, v131
	s_movk_i32 s38, 0xff00
	v_lshlrev_b32_e32 v134, 1, v130
	s_movk_i32 s40, 0x110
	s_movk_i32 s41, 0x1000
	s_mov_b32 s42, 0x42fe0000
	s_mov_b32 s43, 0x40c0c00
	s_movk_i32 s44, 0xff80
	s_mov_b32 s45, 0xff61b1e6
	v_add_u32_e32 v215, s2, v1
	s_mov_b32 s46, 0
	s_mov_b32 s47, s58
	s_branch .LBB0_1207

; #define GAS __attribute__((address_space(1)))
; #define LAS __attribute__((address_space(3)))
; __device__ __forceinline__ unsigned xb_add(unsigned* p, unsigned v) { return __hip_atomic_fetch_add(p, v, __ATOMIC_RELAXED, __HIP_MEMORY_SCOPE_AGENT); }
; __device__ __forceinline__ void xcd_barrier(const XcdBarrier& b) {
;     asm volatile("s_waitcnt vmcnt(0)" ::: "memory");
;     __syncthreads();
;     if (threadIdx.x == 0) {
;         unsigned* bar = b.bar;
;         __builtin_amdgcn_s_waitcnt(0);
;         unsigned nloc = b.st[0], nx = b.st[1];
;         if (nloc == 0u) { xcd_barrier_complete(bar, b.x, nloc, nx); b.st[0] = nloc; b.st[1] = nx; }
;         const unsigned old = xb_add(&bar[XB_XSUB(b.x)], 1u);
;         const unsigned gen = old / nloc;
;         if (old + 1u == (gen + 1u) * nloc) {
; DI void p9v2_phase(Frame& F) {
;     ...
;     for (int tb = (int)blockIdx.x * 64; tb < M; tb += F.G * 64) {
; #pragma unroll
;         for (int j = 0; j < 8; ++j) { const int tl = F.wave * 8 + j;
; #pragma unroll
;             for (int jj = 0; jj < 2; ++jj) *(LAS v4u*)(HQ + tl * 2048 + 1024 * jj + 16 * lane) = *(const GAS v4u*)(F.H2Q + (size_t)(tb + tl) * D + 1024 * jj + 16 * lane); }
.LBB0_1246:
	v_readlane_b32 s84, v252, 13
	v_readlane_b32 s85, v252, 14
	v_mbcnt_lo_u32_b32 v208, -1, 0
	v_mbcnt_hi_u32_b32 v208, -1, v208
	v_lshlrev_b32_e32 v208, 4, v208
	s_nop 3
	s_add_u32 s84, s84, 0x4000000
	s_addc_u32 s85, s85, 0
	s_lshl_b32 s86, s58, 6
	s_lshl_b32 s87, s89, 3
	s_add_i32 s86, s86, s87
	s_lshl_b32 s86, s86, 11
	s_add_u32 s84, s84, s86
	s_addc_u32 s85, s85, 0
	global_load_dwordx4 v[76:79], v208, s[84:85]
	global_load_dwordx4 v[80:83], v208, s[84:85] offset:1024
	global_load_dwordx4 v[84:87], v208, s[84:85] offset:2048
	global_load_dwordx4 v[88:91], v208, s[84:85] offset:3072
	s_add_u32 s84, s84, 0x1000
	s_addc_u32 s85, s85, 0
	global_load_dwordx4 v[92:95], v208, s[84:85]
	global_load_dwordx4 v[96:99], v208, s[84:85] offset:1024
	global_load_dwordx4 v[100:103], v208, s[84:85] offset:2048
	global_load_dwordx4 v[104:107], v208, s[84:85] offset:3072
	s_add_u32 s84, s84, 0x1000
	s_addc_u32 s85, s85, 0
	global_load_dwordx4 v[108:111], v208, s[84:85]
	global_load_dwordx4 v[112:115], v208, s[84:85] offset:1024
	global_load_dwordx4 v[116:119], v208, s[84:85] offset:2048
	global_load_dwordx4 v[120:123], v208, s[84:85] offset:3072
	s_add_u32 s84, s84, 0x1000
	s_addc_u32 s85, s85, 0
	global_load_dwordx4 v[124:127], v208, s[84:85]
	global_load_dwordx4 v[212:215], v208, s[84:85] offset:1024
	global_load_dwordx4 v[216:219], v208, s[84:85] offset:2048
	global_load_dwordx4 v[220:223], v208, s[84:85] offset:3072
	v_readlane_b32 s0, v252, 4
	v_readlane_b32 s1, v252, 5
	s_cmp_gt_i32 s1, 9
	v_readlane_b32 s2, v252, 6
	v_readlane_b32 s3, v252, 7
	s_cselect_b64 s[0:1], -1, 0
	s_and_b64 s[2:3], s[8:9], s[0:1]
	s_andn2_b64 vcc, exec, s[2:3]
	s_cbranch_vccnz .LBB0_1296
	s_waitcnt vmcnt(16)
	v_cmp_eq_u32_e32 vcc, 0, v0
	s_waitcnt lgkmcnt(0)
	s_barrier
	s_and_saveexec_b64 s[2:3], vcc
	s_cbranch_execz .LBB0_1295
	v_readlane_b32 s4, v252, 38
	s_waitcnt vmcnt(0) expcnt(0) lgkmcnt(0)
	s_nop 0
	v_mov_b32_e32 v1, s4
	ds_read_b32 v3, v1
	ds_read_b32 v1, v1 offset:4
	s_waitcnt lgkmcnt(1)
	v_cmp_ne_u32_e32 vcc, 0, v3
	s_cbranch_vccnz .LBB0_1263
	v_readlane_b32 s4, v252, 9
	v_readlane_b32 s5, v252, 10
	s_load_dwordx2 s[8:9], s[4:5], 0x4
	v_readlane_b32 s4, v252, 35
	v_readlane_b32 s5, v252, 36
	s_lshl_b64 s[4:5], s[4:5], 2
	v_readlane_b32 s6, v252, 33
	s_add_u32 s4, s6, s4
	v_readlane_b32 s6, v252, 34
	s_addc_u32 s5, s6, s5
	s_add_u32 s6, s4, 0x1000
	v_readlane_b32 s7, v252, 11
	s_waitcnt lgkmcnt(0)
	s_mul_i32 s30, s8, s7
	s_addc_u32 s7, s5, 0
	s_add_u32 s8, s4, 0x1100
	s_mul_i32 s30, s30, s9
	s_addc_u32 s9, s5, 0
	s_add_u32 s10, s4, 0x1200
	s_addc_u32 s11, s5, 0
	s_add_u32 s12, s4, 0x1300
	s_addc_u32 s13, s5, 0
	s_mov_b32 s31, 1
	v_mov_b32_e32 v17, 0
	s_branch .LBB0_1251

; #define GAS __attribute__((address_space(1)))
; #define LAS __attribute__((address_space(3)))
; DI void p9v2_phase(Frame& F) {
;     ...
;     for (int tb = (int)blockIdx.x * 64; tb < M; tb += F.G * 64) {
; #pragma unroll
;         for (int j = 0; j < 8; ++j) { const int tl = F.wave * 8 + j;
; #pragma unroll
;             for (int jj = 0; jj < 2; ++jj) *(LAS v4u*)(HQ + tl * 2048 + 1024 * jj + 16 * lane) = *(const GAS v4u*)(F.H2Q + (size_t)(tb + tl) * D + 1024 * jj + 16 * lane); }
;         if (tid < 64) SH[tid] = F.SA[tb + tid];
.LBB0_1299:
	s_add_i32 s42, s22, s29
	s_ashr_i32 s43, s42, 31
	s_lshl_b64 s[14:15], s[42:43], 11
	v_lshl_add_u64 v[6:7], v[154:155], 0, s[14:15]
	s_add_i32 s14, s22, s35
	s_ashr_i32 s15, s14, 31
	s_lshl_b64 s[44:45], s[14:15], 11
	v_lshl_add_u64 v[14:15], v[154:155], 0, s[44:45]
	s_add_i32 s44, s22, s48
	s_ashr_i32 s45, s44, 31
	s_lshl_b64 s[44:45], s[44:45], 11
	v_lshl_add_u64 v[22:23], v[154:155], 0, s[44:45]
	s_add_i32 s44, s22, s50
	s_ashr_i32 s45, s44, 31
	s_lshl_b64 s[44:45], s[44:45], 11
	v_lshl_add_u64 v[30:31], v[154:155], 0, s[44:45]
	s_add_i32 s44, s22, s52
	s_ashr_i32 s45, s44, 31
	s_lshl_b64 s[44:45], s[44:45], 11
	s_waitcnt vmcnt(26)
	v_lshl_add_u64 v[38:39], v[154:155], 0, s[44:45]
	s_add_i32 s44, s22, s54
	s_ashr_i32 s45, s44, 31
	s_lshl_b64 s[44:45], s[44:45], 11
	s_waitcnt vmcnt(22)
	v_lshl_add_u64 v[46:47], v[154:155], 0, s[44:45]
	s_add_i32 s44, s22, s56
	s_ashr_i32 s45, s44, 31
	s_lshl_b64 s[44:45], s[44:45], 11
	s_waitcnt vmcnt(15)
	v_lshl_add_u64 v[54:55], v[154:155], 0, s[44:45]
	s_add_i32 s44, s22, s58
	s_ashr_i32 s45, s44, 31
	s_lshl_b64 s[44:45], s[44:45], 11
	s_waitcnt vmcnt(8)
	v_lshl_add_u64 v[62:63], v[154:155], 0, s[44:45]
	s_waitcnt vmcnt(21)
	v_add_u32_e32 v66, s31, v131
	s_waitcnt vmcnt(20)
	v_add_u32_e32 v67, s41, v131
	s_waitcnt vmcnt(19)
	v_add_u32_e32 v68, s49, v131
	s_waitcnt vmcnt(18)
	v_add_u32_e32 v69, s51, v131
	s_waitcnt vmcnt(17)
	v_add_u32_e32 v70, s53, v131
	s_waitcnt vmcnt(16)
	v_add_u32_e32 v71, s55, v131
	v_add_u32_e32 v72, s57, v131
	v_add_u32_e32 v73, s59, v131
	s_waitcnt vmcnt(15)
	ds_write_b128 v66, v[76:79]
	s_waitcnt vmcnt(14)
	ds_write_b128 v66, v[80:83] offset:1024
	s_waitcnt vmcnt(13)
	ds_write_b128 v67, v[84:87]
	s_waitcnt vmcnt(12)
	ds_write_b128 v67, v[88:91] offset:1024
	s_waitcnt vmcnt(11)
	ds_write_b128 v68, v[92:95]
	s_waitcnt vmcnt(10)
	ds_write_b128 v68, v[96:99] offset:1024
	s_waitcnt vmcnt(9)
	ds_write_b128 v69, v[100:103]
	s_waitcnt vmcnt(8)
	ds_write_b128 v69, v[104:107] offset:1024
	s_waitcnt vmcnt(7)
	ds_write_b128 v70, v[108:111]
	s_waitcnt vmcnt(6)
	ds_write_b128 v70, v[112:115] offset:1024
	s_waitcnt vmcnt(5)
	ds_write_b128 v71, v[116:119]
	s_waitcnt vmcnt(4)
	ds_write_b128 v71, v[120:123] offset:1024
	s_waitcnt vmcnt(3)
	ds_write_b128 v72, v[124:127]
	s_waitcnt vmcnt(2)
	ds_write_b128 v72, v[212:215] offset:1024
	s_waitcnt vmcnt(1)
	ds_write_b128 v73, v[216:219]
	s_waitcnt vmcnt(0)
	ds_write_b128 v73, v[220:223] offset:1024
	s_and_saveexec_b64 s[44:45], s[0:1]
	s_cbranch_execz .LBB0_1301
	v_or_b32_e32 v2, s22, v0
	v_ashrrev_i32_e32 v3, 31, v2
	v_lshl_add_u64 v[2:3], v[2:3], 2, s[64:65]
	global_load_dword v2, v[2:3], off
	s_waitcnt vmcnt(0)
	ds_write_b32 v158, v2
